# S4 + MoE gather phase writes only a source-row table; the gate/up GEMM gathers its A rows from the fp8 LayerNorm copy by per-lane LDS-DMA offsets (row copy and its 270 MB of traffic removed); source r
# speedup vs baseline: 1.0105x; 1.0105x over previous
.LBB0_1201:
	v_ashrrev_i32_e32 v13, 6, v12
	v_readlane_b32 s2, v254, 41
	s_add_u32 s16, s20, 0x45900000
	v_and_b32_e32 v36, 63, v12
	v_add_u32_e32 v42, s2, v13
	s_mov_b32 s2, 0x8000
	s_addc_u32 s17, s21, 0
	s_mov_b64 s[50:51], s[16:17]
	v_cmp_gt_i32_e32 vcc, s2, v42
	s_and_saveexec_b64 s[22:23], vcc
	s_cbranch_execz .LBB0_1215
	s_add_u32 s42, s20, 0x260000
	s_addc_u32 s43, s21, 0
	s_add_u32 s44, s20, 0x200000
	s_addc_u32 s45, s21, 0
	v_readlane_b32 s9, v254, 28
	v_ashrrev_i32_e32 v43, 31, v42
	s_add_u32 s2, s20, 0x19900000
	v_lshlrev_b32_e32 v188, 4, v36
	v_lshl_add_u32 v48, v13, 1, s9
	v_lshlrev_b64 v[12:13], 11, v[42:43]
	s_addc_u32 s3, s21, 0
	v_or_b32_e32 v12, v12, v188
	v_lshl_add_u64 v[44:45], s[2:3], 0, v[188:189]
	v_cmp_eq_u32_e32 vcc, 0, v36
	v_lshl_add_u64 v[46:47], s[16:17], 0, v[188:189]
	v_lshl_add_u64 v[50:51], v[42:43], 2, s[44:45]
	v_lshl_add_u64 v[52:53], s[2:3], 0, v[12:13]
	s_mov_b64 s[20:21], 0
	v_mov_b32_e32 v39, v42
	s_branch .LBB0_1204

.LBB0_1204:
	global_load_dword v64, v[50:51], off
	v_add_u32_e32 v69, s66, v39
	s_waitcnt vmcnt(6)
	v_min_i32_e32 v12, 0x7fff, v69
	v_ashrrev_i32_e32 v13, 31, v12
	v_lshl_add_u64 v[14:15], v[12:13], 2, s[44:45]
	s_waitcnt vmcnt(5)
	v_lshlrev_b32_e32 v16, 1, v12
	v_lshlrev_b64 v[12:13], 11, v[12:13]
	v_readlane_b32 s2, v255, 35
	v_lshl_add_u64 v[12:13], v[44:45], 0, v[12:13]
	global_load_dword v124, v189, s[50:51]
	global_load_dword v124, v189, s[50:51]
	v_add_u32_e32 v68, s2, v39
	v_min_i32_e32 v12, 0x7fff, v68
	v_ashrrev_i32_e32 v13, 31, v12
	v_lshlrev_b32_e32 v20, 1, v12
	v_lshl_add_u64 v[18:19], v[12:13], 2, s[44:45]
	v_ashrrev_i32_e32 v21, 31, v20
	v_lshlrev_b64 v[12:13], 11, v[12:13]
	s_mul_i32 s2, s90, 24
	v_ashrrev_i32_e32 v17, 31, v16
	v_lshl_add_u64 v[20:21], v[20:21], 2, s[42:43]
	v_lshl_add_u64 v[12:13], v[44:45], 0, v[12:13]
	v_add_u32_e32 v66, s2, v39
	v_ashrrev_i32_e32 v49, 31, v48
	v_lshl_add_u64 v[16:17], v[16:17], 2, s[42:43]
	global_load_dword v67, v[18:19], off
	global_load_dwordx2 v[56:57], v[20:21], off
	s_nop 0
	global_load_dword v124, v189, s[50:51]
	global_load_dword v124, v189, s[50:51]
	v_min_i32_e32 v12, 0x7fff, v66
	v_lshl_add_u64 v[60:61], v[48:49], 2, s[42:43]
	global_load_dword v49, v[14:15], off
	global_load_dwordx2 v[58:59], v[16:17], off
	global_load_dwordx2 v[62:63], v[60:61], off
	v_lshlrev_b32_e32 v16, 1, v12
	v_ashrrev_i32_e32 v13, 31, v12
	v_ashrrev_i32_e32 v17, 31, v16
	v_lshl_add_u64 v[14:15], v[12:13], 2, s[44:45]
	v_lshl_add_u64 v[16:17], v[16:17], 2, s[42:43]
	v_lshlrev_b64 v[12:13], 11, v[12:13]
	global_load_dword v124, v189, s[50:51]
	global_load_dword v124, v189, s[50:51]
	global_load_dword v43, v[14:15], off
	global_load_dwordx2 v[54:55], v[16:17], off
	v_lshl_add_u64 v[16:17], v[44:45], 0, v[12:13]
	global_load_dword v124, v189, s[50:51]
	s_nop 0
	global_load_dword v124, v189, s[50:51]
	v_mov_b32_e32 v80, 2
	v_readlane_b32 s3, v255, 36
	s_waitcnt vmcnt(15)
	v_lshrrev_b32_e32 v65, 8, v64
	v_cmp_eq_u32_sdwa s[40:41], v64, v242 src0_sel:BYTE_0 src1_sel:DWORD
	s_nop 1
	v_cndmask_b32_e64 v78, 0, v37, s[40:41]
	v_cmp_eq_u32_sdwa s[40:41], v65, v242 src0_sel:BYTE_0 src1_sel:DWORD
	s_nop 1
	v_cndmask_b32_e64 v79, 0, v37, s[40:41]
	v_cmp_eq_u32_sdwa s[40:41], v64, v80 src0_sel:BYTE_0 src1_sel:DWORD
	s_nop 1
	v_cndmask_b32_e64 v78, v78, v38, s[40:41]
	v_cmp_eq_u32_sdwa s[40:41], v65, v80 src0_sel:BYTE_0 src1_sel:DWORD
	v_mov_b32_e32 v80, 3
	s_nop 0
	v_cndmask_b32_e64 v79, v79, v38, s[40:41]
	v_cmp_eq_u32_sdwa s[40:41], v64, v80 src0_sel:BYTE_0 src1_sel:DWORD
	s_nop 1
	v_cndmask_b32_e64 v78, v78, v4, s[40:41]
	v_cmp_eq_u32_sdwa s[40:41], v65, v80 src0_sel:BYTE_0 src1_sel:DWORD
	v_mov_b32_e32 v80, 4
	s_nop 0
	v_cndmask_b32_e64 v79, v79, v4, s[40:41]
	v_cmp_eq_u32_sdwa s[40:41], v64, v80 src0_sel:BYTE_0 src1_sel:DWORD
	s_nop 1
	v_cndmask_b32_e64 v78, v78, v5, s[40:41]
	v_cmp_eq_u32_sdwa s[40:41], v65, v80 src0_sel:BYTE_0 src1_sel:DWORD
	v_mov_b32_e32 v80, 5
	s_nop 0
	v_cndmask_b32_e64 v79, v79, v5, s[40:41]
	v_cmp_eq_u32_sdwa s[40:41], v64, v80 src0_sel:BYTE_0 src1_sel:DWORD
	s_nop 1
	v_cndmask_b32_e64 v78, v78, v6, s[40:41]
	v_cmp_eq_u32_sdwa s[40:41], v65, v80 src0_sel:BYTE_0 src1_sel:DWORD
	v_mov_b32_e32 v80, 6
	s_nop 0
	v_cndmask_b32_e64 v79, v79, v6, s[40:41]
	v_cmp_eq_u32_sdwa s[40:41], v64, v80 src0_sel:BYTE_0 src1_sel:DWORD
	s_nop 1
	v_cndmask_b32_e64 v78, v78, v7, s[40:41]
	v_cmp_eq_u32_sdwa s[40:41], v65, v80 src0_sel:BYTE_0 src1_sel:DWORD
	v_mov_b32_e32 v80, 7
	s_nop 0
	v_cndmask_b32_e64 v79, v79, v7, s[40:41]
	v_cmp_eq_u32_sdwa s[40:41], v64, v80 src0_sel:BYTE_0 src1_sel:DWORD
	s_nop 1
	v_cndmask_b32_e64 v64, v78, v40, s[40:41]
	v_cmp_eq_u32_sdwa s[40:41], v65, v80 src0_sel:BYTE_0 src1_sel:DWORD
	s_waitcnt vmcnt(6)
	v_lshl_add_u32 v62, v64, 8, v62
	v_cndmask_b32_e64 v65, v79, v40, s[40:41]
	v_lshl_add_u32 v64, v65, 8, v63
	v_ashrrev_i32_e32 v63, 31, v62
	v_lshlrev_b64 v[78:79], 11, v[62:63]
	v_ashrrev_i32_e32 v65, 31, v64
	v_lshlrev_b64 v[80:81], 11, v[64:65]
	v_lshl_add_u64 v[78:79], v[46:47], 0, v[78:79]
	s_waitcnt vmcnt(4)
	v_lshlrev_b32_e32 v120, 2, v62
	v_lshlrev_b32_e32 v121, 2, v64
	global_store_dword v120, v39, s[50:51]
	global_store_dword v120, v39, s[50:51]
	v_lshl_add_u64 v[78:79], v[46:47], 0, v[80:81]
	global_store_dword v121, v39, s[50:51]
	global_store_dword v121, v39, s[50:51]
	s_and_saveexec_b64 s[40:41], vcc
	s_cbranch_execz .LBB0_1206
	v_mov_b32_e32 v63, v64
	global_store_dwordx2 v[60:61], v[62:63], off
.LBB0_1206:
	s_or_b64 exec, exec, s[40:41]
	s_mov_b32 s2, 0x8000
	v_cmp_gt_i32_e64 s[40:41], s2, v69
	s_and_saveexec_b64 s[46:47], s[40:41]
	s_cbranch_execz .LBB0_1209
	v_lshrrev_b32_e32 v60, 8, v49
	v_cmp_eq_u32_sdwa s[40:41], v49, v242 src0_sel:BYTE_0 src1_sel:DWORD
	v_mov_b32_e32 v63, 2
	s_nop 0
	v_cndmask_b32_e64 v61, 0, v37, s[40:41]
	v_cmp_eq_u32_sdwa s[40:41], v60, v242 src0_sel:BYTE_0 src1_sel:DWORD
	s_nop 1
	v_cndmask_b32_e64 v62, 0, v37, s[40:41]
	v_cmp_eq_u32_sdwa s[40:41], v60, v63 src0_sel:BYTE_0 src1_sel:DWORD
	s_nop 1
	v_cndmask_b32_e64 v62, v62, v38, s[40:41]
	v_cmp_eq_u32_sdwa s[40:41], v49, v63 src0_sel:BYTE_0 src1_sel:DWORD
	v_mov_b32_e32 v63, 3
	s_nop 0
	v_cndmask_b32_e64 v61, v61, v38, s[40:41]
	v_cmp_eq_u32_sdwa s[40:41], v49, v63 src0_sel:BYTE_0 src1_sel:DWORD
	s_nop 1
	v_cndmask_b32_e64 v61, v61, v4, s[40:41]
	v_cmp_eq_u32_sdwa s[40:41], v60, v63 src0_sel:BYTE_0 src1_sel:DWORD
	v_mov_b32_e32 v63, 4
	s_nop 0
	v_cndmask_b32_e64 v62, v62, v4, s[40:41]
	v_cmp_eq_u32_sdwa s[40:41], v60, v63 src0_sel:BYTE_0 src1_sel:DWORD
	s_nop 1
	v_cndmask_b32_e64 v62, v62, v5, s[40:41]
	v_cmp_eq_u32_sdwa s[40:41], v49, v63 src0_sel:BYTE_0 src1_sel:DWORD
	v_mov_b32_e32 v63, 5
	s_nop 0
	v_cndmask_b32_e64 v61, v61, v5, s[40:41]
	v_cmp_eq_u32_sdwa s[40:41], v49, v63 src0_sel:BYTE_0 src1_sel:DWORD
	s_nop 1
	v_cndmask_b32_e64 v61, v61, v6, s[40:41]
	v_cmp_eq_u32_sdwa s[40:41], v60, v63 src0_sel:BYTE_0 src1_sel:DWORD
	v_mov_b32_e32 v63, 6
	s_nop 0
	v_cndmask_b32_e64 v62, v62, v6, s[40:41]
	v_cmp_eq_u32_sdwa s[40:41], v60, v63 src0_sel:BYTE_0 src1_sel:DWORD
	s_nop 1
	v_cndmask_b32_e64 v62, v62, v7, s[40:41]
	v_cmp_eq_u32_sdwa s[40:41], v49, v63 src0_sel:BYTE_0 src1_sel:DWORD
	v_mov_b32_e32 v63, 7
	s_nop 0
	v_cndmask_b32_e64 v61, v61, v7, s[40:41]
	v_cmp_eq_u32_sdwa s[40:41], v49, v63 src0_sel:BYTE_0 src1_sel:DWORD
	s_nop 1
	v_cndmask_b32_e64 v49, v61, v40, s[40:41]
	v_cmp_eq_u32_sdwa s[40:41], v60, v63 src0_sel:BYTE_0 src1_sel:DWORD
	v_lshl_add_u32 v58, v49, 8, v58
	s_nop 0
	v_cndmask_b32_e64 v60, v62, v40, s[40:41]
	v_lshl_add_u32 v60, v60, 8, v59
	v_ashrrev_i32_e32 v59, 31, v58
	v_lshlrev_b64 v[62:63], 11, v[58:59]
	v_ashrrev_i32_e32 v61, 31, v60
	v_lshlrev_b64 v[64:65], 11, v[60:61]
	v_lshl_add_u64 v[62:63], v[46:47], 0, v[62:63]
	v_lshlrev_b32_e32 v120, 2, v58
	v_lshlrev_b32_e32 v121, 2, v60
	global_store_dword v120, v69, s[50:51]
	global_store_dword v120, v69, s[50:51]
	v_lshl_add_u64 v[62:63], v[46:47], 0, v[64:65]
	global_store_dword v121, v69, s[50:51]
	global_store_dword v121, v69, s[50:51]
	s_and_b64 exec, exec, vcc
	s_cbranch_execz .LBB0_1209
	v_readlane_b32 s2, v255, 35
	v_mov_b32_e32 v59, v60
	v_readlane_b32 s3, v255, 36
	v_add_u32_e32 v28, s2, v48
	v_ashrrev_i32_e32 v29, 31, v28
	v_lshl_add_u64 v[28:29], v[28:29], 2, s[42:43]
	global_store_dwordx2 v[28:29], v[58:59], off
.LBB0_1209:
	s_or_b64 exec, exec, s[46:47]
	s_mov_b32 s2, 0x8000
	v_cmp_gt_i32_e64 s[40:41], s2, v68
	s_and_saveexec_b64 s[46:47], s[40:41]
	s_cbranch_execz .LBB0_1212
	v_lshrrev_b32_e32 v28, 8, v67
	v_cmp_eq_u32_sdwa s[40:41], v67, v242 src0_sel:BYTE_0 src1_sel:DWORD
	v_mov_b32_e32 v31, 2
	s_nop 0
	v_cndmask_b32_e64 v29, 0, v37, s[40:41]
	v_cmp_eq_u32_sdwa s[40:41], v28, v242 src0_sel:BYTE_0 src1_sel:DWORD
	s_nop 1
	v_cndmask_b32_e64 v30, 0, v37, s[40:41]
	v_cmp_eq_u32_sdwa s[40:41], v28, v31 src0_sel:BYTE_0 src1_sel:DWORD
	s_nop 1
	v_cndmask_b32_e64 v30, v30, v38, s[40:41]
	v_cmp_eq_u32_sdwa s[40:41], v67, v31 src0_sel:BYTE_0 src1_sel:DWORD
	v_mov_b32_e32 v31, 3
	s_nop 0
	v_cndmask_b32_e64 v29, v29, v38, s[40:41]
	v_cmp_eq_u32_sdwa s[40:41], v67, v31 src0_sel:BYTE_0 src1_sel:DWORD
	s_nop 1
	v_cndmask_b32_e64 v29, v29, v4, s[40:41]
	v_cmp_eq_u32_sdwa s[40:41], v28, v31 src0_sel:BYTE_0 src1_sel:DWORD
	v_mov_b32_e32 v31, 4
	s_nop 0
	v_cndmask_b32_e64 v30, v30, v4, s[40:41]
	v_cmp_eq_u32_sdwa s[40:41], v28, v31 src0_sel:BYTE_0 src1_sel:DWORD
	s_nop 1
	v_cndmask_b32_e64 v30, v30, v5, s[40:41]
	v_cmp_eq_u32_sdwa s[40:41], v67, v31 src0_sel:BYTE_0 src1_sel:DWORD
	v_mov_b32_e32 v31, 5
	s_nop 0
	v_cndmask_b32_e64 v29, v29, v5, s[40:41]
	v_cmp_eq_u32_sdwa s[40:41], v67, v31 src0_sel:BYTE_0 src1_sel:DWORD
	s_nop 1
	v_cndmask_b32_e64 v29, v29, v6, s[40:41]
	v_cmp_eq_u32_sdwa s[40:41], v28, v31 src0_sel:BYTE_0 src1_sel:DWORD
	v_mov_b32_e32 v31, 6
	s_nop 0
	v_cndmask_b32_e64 v30, v30, v6, s[40:41]
	v_cmp_eq_u32_sdwa s[40:41], v28, v31 src0_sel:BYTE_0 src1_sel:DWORD
	s_nop 1
	v_cndmask_b32_e64 v30, v30, v7, s[40:41]
	v_cmp_eq_u32_sdwa s[40:41], v67, v31 src0_sel:BYTE_0 src1_sel:DWORD
	v_mov_b32_e32 v31, 7
	s_nop 0
	v_cndmask_b32_e64 v29, v29, v7, s[40:41]
	v_cmp_eq_u32_sdwa s[40:41], v67, v31 src0_sel:BYTE_0 src1_sel:DWORD
	s_nop 1
	v_cndmask_b32_e64 v29, v29, v40, s[40:41]
	v_cmp_eq_u32_sdwa s[40:41], v28, v31 src0_sel:BYTE_0 src1_sel:DWORD
	s_nop 1
	v_cndmask_b32_e64 v28, v30, v40, s[40:41]
	v_lshl_add_u32 v30, v28, 8, v57
	v_lshl_add_u32 v28, v29, 8, v56
	v_ashrrev_i32_e32 v29, 31, v28
	v_lshlrev_b64 v[32:33], 11, v[28:29]
	v_ashrrev_i32_e32 v31, 31, v30
	v_lshlrev_b64 v[34:35], 11, v[30:31]
	v_lshl_add_u64 v[32:33], v[46:47], 0, v[32:33]
	v_lshlrev_b32_e32 v120, 2, v28
	v_lshlrev_b32_e32 v121, 2, v30
	global_store_dword v120, v68, s[50:51]
	global_store_dword v120, v68, s[50:51]
	v_lshl_add_u64 v[32:33], v[46:47], 0, v[34:35]
	global_store_dword v121, v68, s[50:51]
	global_store_dword v121, v68, s[50:51]
	s_and_b64 exec, exec, vcc
	s_cbranch_execz .LBB0_1212
	v_readlane_b32 s2, v255, 29
	v_mov_b32_e32 v29, v30
	v_readlane_b32 s3, v255, 30
	v_add_u32_e32 v20, s2, v48
	v_ashrrev_i32_e32 v21, 31, v20
	v_lshl_add_u64 v[20:21], v[20:21], 2, s[42:43]
	global_store_dwordx2 v[20:21], v[28:29], off
.LBB0_1212:
	s_or_b64 exec, exec, s[46:47]
	s_mov_b32 s2, 0x8000
	v_cmp_gt_i32_e64 s[40:41], s2, v66
	s_and_saveexec_b64 s[46:47], s[40:41]
	s_cbranch_execz .LBB0_1203
	s_waitcnt vmcnt(7)
	v_lshrrev_b32_e32 v20, 8, v43
	v_cmp_eq_u32_sdwa s[40:41], v43, v242 src0_sel:BYTE_0 src1_sel:DWORD
	v_mov_b32_e32 v23, 2
	s_nop 0
	v_cndmask_b32_e64 v21, 0, v37, s[40:41]
	v_cmp_eq_u32_sdwa s[40:41], v20, v242 src0_sel:BYTE_0 src1_sel:DWORD
	s_nop 1
	v_cndmask_b32_e64 v22, 0, v37, s[40:41]
	v_cmp_eq_u32_sdwa s[40:41], v20, v23 src0_sel:BYTE_0 src1_sel:DWORD
	s_nop 1
	v_cndmask_b32_e64 v22, v22, v38, s[40:41]
	v_cmp_eq_u32_sdwa s[40:41], v43, v23 src0_sel:BYTE_0 src1_sel:DWORD
	v_mov_b32_e32 v23, 3
	s_nop 0
	v_cndmask_b32_e64 v21, v21, v38, s[40:41]
	v_cmp_eq_u32_sdwa s[40:41], v43, v23 src0_sel:BYTE_0 src1_sel:DWORD
	s_nop 1
	v_cndmask_b32_e64 v21, v21, v4, s[40:41]
	v_cmp_eq_u32_sdwa s[40:41], v20, v23 src0_sel:BYTE_0 src1_sel:DWORD
	v_mov_b32_e32 v23, 4
	s_nop 0
	v_cndmask_b32_e64 v22, v22, v4, s[40:41]
	v_cmp_eq_u32_sdwa s[40:41], v20, v23 src0_sel:BYTE_0 src1_sel:DWORD
	s_nop 1
	v_cndmask_b32_e64 v22, v22, v5, s[40:41]
	v_cmp_eq_u32_sdwa s[40:41], v43, v23 src0_sel:BYTE_0 src1_sel:DWORD
	v_mov_b32_e32 v23, 5
	s_nop 0
	v_cndmask_b32_e64 v21, v21, v5, s[40:41]
	v_cmp_eq_u32_sdwa s[40:41], v43, v23 src0_sel:BYTE_0 src1_sel:DWORD
	s_nop 1
	v_cndmask_b32_e64 v21, v21, v6, s[40:41]
	v_cmp_eq_u32_sdwa s[40:41], v20, v23 src0_sel:BYTE_0 src1_sel:DWORD
	v_mov_b32_e32 v23, 6
	s_nop 0
	v_cndmask_b32_e64 v22, v22, v6, s[40:41]
	v_cmp_eq_u32_sdwa s[40:41], v20, v23 src0_sel:BYTE_0 src1_sel:DWORD
	s_nop 1
	v_cndmask_b32_e64 v22, v22, v7, s[40:41]
	v_cmp_eq_u32_sdwa s[40:41], v43, v23 src0_sel:BYTE_0 src1_sel:DWORD
	v_mov_b32_e32 v23, 7
	s_nop 0
	v_cndmask_b32_e64 v21, v21, v7, s[40:41]
	v_cmp_eq_u32_sdwa s[40:41], v43, v23 src0_sel:BYTE_0 src1_sel:DWORD
	s_nop 1
	v_cndmask_b32_e64 v21, v21, v40, s[40:41]
	v_cmp_eq_u32_sdwa s[40:41], v20, v23 src0_sel:BYTE_0 src1_sel:DWORD
	s_nop 1
	v_cndmask_b32_e64 v20, v22, v40, s[40:41]
	s_waitcnt vmcnt(6)
	v_lshl_add_u32 v22, v20, 8, v55
	v_lshl_add_u32 v20, v21, 8, v54
	v_ashrrev_i32_e32 v21, 31, v20
	v_lshlrev_b64 v[24:25], 11, v[20:21]
	v_ashrrev_i32_e32 v23, 31, v22
	v_lshlrev_b64 v[26:27], 11, v[22:23]
	v_lshl_add_u64 v[24:25], v[46:47], 0, v[24:25]
	s_waitcnt vmcnt(5)
	v_lshlrev_b32_e32 v120, 2, v20
	v_lshlrev_b32_e32 v121, 2, v22
	global_store_dword v120, v66, s[50:51]
	s_waitcnt vmcnt(5)
	global_store_dword v120, v66, s[50:51]
	v_lshl_add_u64 v[24:25], v[46:47], 0, v[26:27]
	global_store_dword v121, v66, s[50:51]
	global_store_dword v121, v66, s[50:51]
	s_and_b64 exec, exec, vcc
	s_cbranch_execz .LBB0_1203
	s_mul_i32 s2, s90, 48
	v_add_u32_e32 v12, s2, v48
	v_ashrrev_i32_e32 v13, 31, v12
	v_mov_b32_e32 v21, v22
	v_lshl_add_u64 v[12:13], v[12:13], 2, s[42:43]
	global_store_dwordx2 v[12:13], v[20:21], off
	s_branch .LBB0_1203

.LBB0_1217:
	s_mov_b32 s72, s73
	v_add_u32_e32 v12, s66, v12
	v_mov_b64_e32 v[18:19], s[72:73]
	v_cmp_ge_i32_e32 vcc, v12, v16
	v_subrev_u32_e32 v122, s50, v14
	v_lshrrev_b32_e32 v122, 9, v122
	v_mov_b32_e32 v123, 0
	global_store_dword v122, v123, s[50:51]
	s_or_b64 s[22:23], vcc, s[22:23]
	v_lshl_add_u64 v[14:15], v[14:15], 0, s[68:69]
	s_andn2_b64 exec, exec, s[22:23]
	s_cbranch_execnz .LBB0_1217

.LBB0_1220:
	s_mov_b32 s72, s73
	v_add_u32_e32 v8, s66, v8
	v_mov_b64_e32 v[16:17], s[72:73]
	v_cmp_ge_i32_e32 vcc, v8, v14
	v_subrev_u32_e32 v122, s50, v12
	v_lshrrev_b32_e32 v122, 9, v122
	v_mov_b32_e32 v123, 0
	global_store_dword v122, v123, s[50:51]
	s_or_b64 s[22:23], vcc, s[22:23]
	v_lshl_add_u64 v[12:13], v[12:13], 0, s[68:69]
	s_andn2_b64 exec, exec, s[22:23]
	s_cbranch_execnz .LBB0_1220

.LBB0_1223:
	s_mov_b32 s72, s73
	v_add_u32_e32 v8, s66, v8
	v_mov_b64_e32 v[14:15], s[72:73]
	v_cmp_ge_i32_e32 vcc, v8, v4
	v_subrev_u32_e32 v122, s50, v12
	v_lshrrev_b32_e32 v122, 9, v122
	v_mov_b32_e32 v123, 0
	global_store_dword v122, v123, s[50:51]
	s_or_b64 s[22:23], vcc, s[22:23]
	v_lshl_add_u64 v[12:13], v[12:13], 0, s[68:69]
	s_andn2_b64 exec, exec, s[22:23]
	s_cbranch_execnz .LBB0_1223

.LBB0_1226:
	s_mov_b32 s72, s73
	v_add_u32_e32 v4, s66, v4
	v_mov_b64_e32 v[12:13], s[72:73]
	v_cmp_ge_i32_e32 vcc, v4, v10
	v_subrev_u32_e32 v122, s50, v8
	v_lshrrev_b32_e32 v122, 9, v122
	v_mov_b32_e32 v123, 0
	global_store_dword v122, v123, s[50:51]
	s_or_b64 s[22:23], vcc, s[22:23]
	v_lshl_add_u64 v[8:9], v[8:9], 0, s[68:69]
	s_andn2_b64 exec, exec, s[22:23]
	s_cbranch_execnz .LBB0_1226

.LBB0_1229:
	s_mov_b32 s72, s73
	v_add_u32_e32 v4, s66, v4
	v_mov_b64_e32 v[10:11], s[72:73]
	v_cmp_ge_i32_e32 vcc, v4, v6
	v_subrev_u32_e32 v122, s50, v8
	v_lshrrev_b32_e32 v122, 9, v122
	v_mov_b32_e32 v123, 0
	global_store_dword v122, v123, s[50:51]
	s_or_b64 s[22:23], vcc, s[22:23]
	v_lshl_add_u64 v[8:9], v[8:9], 0, s[68:69]
	s_andn2_b64 exec, exec, s[22:23]
	s_cbranch_execnz .LBB0_1229

.LBB0_1232:
	s_mov_b32 s72, s73
	v_add_u32_e32 v0, s66, v0
	v_mov_b64_e32 v[8:9], s[72:73]
	v_cmp_ge_i32_e32 vcc, v0, v7
	v_subrev_u32_e32 v122, s50, v4
	v_lshrrev_b32_e32 v122, 9, v122
	v_mov_b32_e32 v123, 0
	global_store_dword v122, v123, s[50:51]
	s_or_b64 s[22:23], vcc, s[22:23]
	v_lshl_add_u64 v[4:5], v[4:5], 0, s[68:69]
	s_andn2_b64 exec, exec, s[22:23]
	s_cbranch_execnz .LBB0_1232

.LBB0_1235:
	s_mov_b32 s72, s73
	v_add_u32_e32 v0, s66, v0
	v_mov_b64_e32 v[8:9], s[72:73]
	v_cmp_ge_i32_e32 vcc, v0, v6
	v_subrev_u32_e32 v122, s50, v4
	v_lshrrev_b32_e32 v122, 9, v122
	v_mov_b32_e32 v123, 0
	global_store_dword v122, v123, s[50:51]
	s_or_b64 s[22:23], vcc, s[22:23]
	v_lshl_add_u64 v[4:5], v[4:5], 0, s[68:69]
	s_andn2_b64 exec, exec, s[22:23]
	s_cbranch_execnz .LBB0_1235

.LBB0_1238:
	s_mov_b32 s72, s73
	v_add_u32_e32 v0, s66, v0
	v_mov_b64_e32 v[6:7], s[72:73]
	v_cmp_ge_i32_e32 vcc, v0, v4
	v_subrev_u32_e32 v122, s50, v2
	v_lshrrev_b32_e32 v122, 9, v122
	v_mov_b32_e32 v123, 0
	global_store_dword v122, v123, s[50:51]
	s_or_b64 s[16:17], vcc, s[16:17]
	v_lshl_add_u64 v[2:3], v[2:3], 0, s[68:69]
	s_andn2_b64 exec, exec, s[16:17]
	s_cbranch_execnz .LBB0_1238

.LBB0_1296:
	v_readlane_b32 s0, v253, 2
	v_readlane_b32 s1, v253, 3
	s_load_dwordx2 s[0:1], s[0:1], 0xf8
	v_readlane_b32 s20, v253, 6
	v_readlane_b32 s22, v253, 8
	v_readlane_b32 s23, v253, 9
	s_mov_b64 s[10:11], s[22:23]
	s_waitcnt lgkmcnt(0)
	global_load_dword v0, v189, s[0:1] offset:512 sc1
	v_readlane_b32 s0, v255, 47
	s_add_i32 s2, s0, 10
	s_cmp_lt_i32 s2, s11
	v_mov_b32_e32 v1, 0x108
	s_cselect_b64 s[0:1], -1, 0
	s_cmp_gt_i32 s10, s3
	v_readlane_b32 s21, v253, 7
	s_waitcnt vmcnt(0)
	v_readfirstlane_b32 s3, v0
	v_med3_i32 v0, v0, 0, v1
	s_nop 0
	v_readfirstlane_b32 s27, v0
	s_cbranch_scc1 .LBB0_1372
	s_cmp_gt_i32 s3, 0
	s_cselect_b64 s[10:11], -1, 0
	s_and_b64 s[10:11], s[16:17], s[10:11]
	s_andn2_b64 vcc, exec, s[10:11]
	s_cbranch_vccnz .LBB0_1316
	v_readlane_b32 s10, v253, 2
	v_readlane_b32 s11, v253, 3
	s_load_dwordx2 s[16:17], s[10:11], 0xf8
	v_mov_b32_e32 v0, 0x1000
	s_mul_i32 s13, s27, 56
	v_readlane_b32 s10, v255, 14
	s_waitcnt lgkmcnt(0)
	global_load_dword v1, v0, s[16:17] offset:24 sc1
	global_load_dword v2, v0, s[16:17] offset:28 sc1
	global_load_dwordx2 v[4:5], v0, s[16:17] offset:80 sc1
	v_mbcnt_lo_u32_b32 v0, -1, 0
	v_mbcnt_hi_u32_b32 v0, -1, v0
	s_cmp_ge_i32 s10, s13
	v_or_b32_e32 v0, s33, v0
	v_readlane_b32 s11, v255, 15
	v_readfirstlane_b32 s9, v0
	s_waitcnt vmcnt(0)
	v_readfirstlane_b32 s40, v4
	v_readfirstlane_b32 s41, v5
	s_cbranch_scc1 .LBB0_1316
	v_bfe_i32 v5, v0, 27, 1
	v_lshlrev_b32_e32 v3, 4, v0
	v_lshrrev_b32_e32 v5, 22, v5
	v_add_u32_e32 v5, v3, v5
	v_and_b32_e32 v5, 0xfffffc00, v5
	v_sub_u32_e32 v5, v3, v5
	v_ashrrev_i32_e32 v4, 31, v0
	v_lshrrev_b32_e32 v6, 4, v5
	v_lshrrev_b32_e32 v4, 26, v4
	v_bitop3_b32 v6, v6, v5, 32 bitop3:0x6c
	v_ashrrev_i32_e32 v5, 31, v5
	v_add_u32_e32 v4, v0, v4
	v_lshrrev_b32_e32 v5, 26, v5
	v_ashrrev_i32_e32 v4, 6, v4
	v_add_u32_e32 v5, v6, v5
	v_lshlrev_b32_e32 v7, 3, v4
	v_ashrrev_i32_e32 v5, 6, v5
	v_and_b32_e32 v7, -16, v7
	v_mul_i32_i24_e32 v8, 64, v5
	v_add_u32_e32 v7, v5, v7
	v_sub_u32_e32 v6, v6, v8
	v_lshlrev_b32_e32 v4, 5, v4
	v_ashrrev_i16_sdwa v6, v242, sext(v6) dst_sel:DWORD dst_unused:UNUSED_PAD src0_sel:DWORD src1_sel:BYTE_0
	v_lshlrev_b32_e32 v8, 1, v7
	v_lshrrev_b32_e32 v9, 2, v7
	v_and_b32_e32 v5, 3, v5
	s_mov_b32 s11, 0x1fffe0
	v_and_b32_e32 v4, 32, v4
	v_bfe_i32 v6, v6, 0, 16
	v_and_b32_e32 v8, 24, v8
	v_and_b32_e32 v9, 4, v9
	v_and_or_b32 v5, v7, s11, v5
	v_or3_b32 v5, v5, v9, v8
	v_add_lshl_u32 v4, v4, v6, 1
	v_add_u32_e32 v3, 0x2000, v3
	v_lshl_add_u32 v132, v7, 11, v4
	v_lshl_add_u32 v133, v5, 11, v4
	v_ashrrev_i32_e32 v4, 31, v3
	v_lshrrev_b32_e32 v4, 22, v4
	v_add_u32_e32 v4, v3, v4
	v_ashrrev_i32_e32 v4, 10, v4
	v_mul_i32_i24_e32 v5, 0x400, v4
	v_sub_u32_e32 v3, v3, v5
	v_lshrrev_b32_e32 v5, 4, v3
	v_bitop3_b32 v3, v5, v3, 32 bitop3:0x6c
	v_ashrrev_i32_e32 v6, 31, v3
	v_lshrrev_b32_e32 v6, 26, v6
	s_add_u32 s18, s16, 0x45900000
	v_lshlrev_b32_e32 v5, 3, v4
	v_add_u32_e32 v6, v3, v6
	v_writelane_b32 v255, s28, 48
	s_addc_u32 s19, s17, 0
	v_and_b32_e32 v5, -16, v5
	v_ashrrev_i32_e32 v7, 6, v6
	v_writelane_b32 v255, s29, 49
	s_add_u32 s28, s16, 0xb900000
	v_add_u32_e32 v5, v7, v5
	v_and_b32_e32 v7, 3, v7
	s_addc_u32 s29, s17, 0
	v_and_or_b32 v7, v5, s11, v7
	s_ashr_i32 s11, s9, 6
	s_lshr_b32 s30, s13, 3
	v_readlane_b32 s20, v254, 54
	s_ashr_i32 s10, s9, 8
	s_lshl_b32 s12, s11, 10
	s_add_i32 s31, s30, 1
	v_readlane_b32 s21, v254, 55
	s_and_b64 s[20:21], s[20:21], exec
	s_cselect_b32 s20, s31, s30
	v_readlane_b32 s21, v255, 0
	s_mul_i32 s20, s20, s21
	v_readlane_b32 s21, v255, 3
	s_add_i32 s20, s20, s21
	s_mul_hi_i32 s21, s20, 0x92492493
	s_add_i32 s21, s21, s20
	s_lshr_b32 s22, s21, 31
	s_ashr_i32 s21, s21, 8
	s_add_i32 s21, s21, s22
	v_and_b32_e32 v6, 0xc0, v6
	s_lshl_b32 s22, s21, 3
	v_sub_u32_e32 v3, v3, v6
	s_sub_i32 s23, s27, s22
	v_lshlrev_b32_e32 v4, 5, v4
	v_ashrrev_i16_sdwa v3, v242, sext(v3) dst_sel:DWORD dst_unused:UNUSED_PAD src0_sel:DWORD src1_sel:BYTE_0
	s_min_i32 s23, s23, 8
	s_mulk_i32 s21, 0x1c0
	v_and_b32_e32 v4, 32, v4
	v_bfe_i32 v3, v3, 0, 16
	s_sub_i32 s34, s20, s21
	s_sext_i32_i16 s20, s23
	v_add_lshl_u32 v3, v4, v3, 1
	v_cvt_f32_i32_e32 v4, s20
	v_lshlrev_b32_e32 v6, 1, v5
	v_lshrrev_b32_e32 v8, 2, v5
	v_and_b32_e32 v6, 24, v6
	v_and_b32_e32 v8, 4, v8
	v_or3_b32 v6, v7, v8, v6
	v_lshl_add_u32 v134, v5, 11, v3
	v_lshrrev_b32_e32 v232, 9, v132
	v_and_b32_e32 v232, -4, v232
	v_lshrrev_b32_e32 v233, 9, v134
	v_and_b32_e32 v233, -4, v233
	v_and_b32_e32 v234, 0x7ff, v132
	v_add_u32_e32 v234, 0x19900000, v234
	v_and_b32_e32 v235, 0x7ff, v134
	v_add_u32_e32 v235, 0x19900000, v235
	v_lshl_add_u32 v135, v6, 11, v3
	v_cvt_f32_i32_e32 v3, s34
	v_rcp_iflag_f32_e32 v5, v4
	s_xor_b32 s21, s34, s20
	s_ashr_i32 s21, s21, 30
	s_or_b32 s35, s21, 1
	v_mul_f32_e32 v5, v3, v5
	v_trunc_f32_e32 v5, v5
	v_fma_f32 v3, -v5, v4, v3
	v_cvt_i32_f32_e32 v5, v5
	v_cmp_ge_f32_e64 s[20:21], |v3|, |v4|
	s_and_b64 s[20:21], s[20:21], exec
	s_cselect_b32 s20, s35, 0
	v_readfirstlane_b32 s21, v5
	s_add_i32 s20, s21, s20
	s_sext_i32_i16 s85, s20
	s_mul_i32 s20, s20, s23
	s_sub_i32 s20, s34, s20
	s_sext_i32_i16 s20, s20
	s_add_i32 s52, s22, s20
	s_ashr_i32 s53, s52, 31
	s_lshl_b64 s[20:21], s[52:53], 2
	s_add_u32 s20, s16, s20
	s_addc_u32 s21, s17, s21
	global_load_dword v3, v189, s[20:21] offset:768
	s_lshl_b32 s92, s52, 10
	s_add_u32 s20, s18, s92
	s_addc_u32 s21, s19, 0
	global_load_dword v220, v232, s[20:21]
	global_load_dword v221, v233, s[20:21]
	global_load_dword v222, v232, s[20:21] offset:512
	global_load_dword v223, v233, s[20:21] offset:512
	s_lshl_b64 s[22:23], s[52:53], 19
	s_waitcnt vmcnt(0)
	s_lshl_b32 s92, s52, 19
	v_lshl_add_u32 v220, v220, 11, v234
	v_lshl_add_u32 v221, v221, 11, v235
	v_lshl_add_u32 v222, v222, 11, v234
	v_lshl_add_u32 v223, v223, 11, v235
	v_subrev_u32_e32 v220, s92, v220
	v_subrev_u32_e32 v221, s92, v221
	s_add_i32 s92, s92, 0x40000
	v_subrev_u32_e32 v222, s92, v222
	v_subrev_u32_e32 v223, s92, v223
	v_mov_b32_e32 v224, v220
	v_mov_b32_e32 v225, v221
	v_mov_b32_e32 v226, v222
	v_mov_b32_e32 v227, v223
	v_readfirstlane_b32 s20, v3
	s_mul_i32 s20, s20, 56
	s_add_i32 s20, s20, s85
	s_ashr_i32 s21, s20, 31
	s_lshl_b64 s[20:21], s[20:21], 19
	s_add_u32 s54, s28, s20
	s_addc_u32 s55, s29, s21
	s_add_i32 s34, s12, 0
	s_add_i32 s35, s34, 0x10000
	s_mov_b32 m0, s35
	s_nop 0
	global_load_lds_dwordx4 v133, s[54:55]
	s_add_i32 s36, s34, 0x12000
	s_mov_b32 m0, s36
	s_nop 0
	global_load_lds_dwordx4 v135, s[54:55]
	s_add_u32 s20, s54, 0x40000
	s_addc_u32 s21, s55, 0
	s_add_i32 s37, s34, 0x14000
	s_mov_b32 m0, s37
	s_nop 0
	global_load_lds_dwordx4 v133, s[20:21]
	s_add_i32 s65, s34, 0x16000
	s_mov_b32 m0, s65
	s_nop 0
	global_load_lds_dwordx4 v135, s[20:21]
	s_add_u32 s56, s16, s22
	s_addc_u32 s57, s17, s23
	s_mov_b32 m0, s34
	s_nop 0
	global_load_lds_dwordx4 v220, s[56:57]
	s_add_i32 s66, s34, 0x2000
	s_mov_b32 m0, s66
	s_nop 0
	global_load_lds_dwordx4 v221, s[56:57]
	s_add_u32 s20, s56, 0x40000
	s_addc_u32 s21, s57, 0
	s_add_i32 s67, s34, 0x4000
	s_mov_b32 m0, s67
	s_nop 0
	global_load_lds_dwordx4 v222, s[20:21]
	s_add_i32 s68, s34, 0x6000
	s_mov_b32 m0, s68
	s_nop 0
	global_load_lds_dwordx4 v223, s[20:21]
	s_cmp_eq_u32 s10, 1
	s_cselect_b64 s[20:21], -1, 0
	s_cmp_lg_u32 s10, 1
	s_cbranch_scc1 .LBB0_1301
	s_barrier
.LBB0_1301:
	s_add_u32 s22, s16, 0x56100000
	s_flbit_i32_b32 s12, s41
	s_addc_u32 s23, s17, 0
	s_min_u32 s12, s12, 32
	s_lshl_b64 s[40:41], s[40:41], s12
	s_min_u32 s40, s40, 1
	v_fmac_f32_e32 v2, 0x40880000, v1
	s_or_b32 s40, s41, s40
	v_max_f32_e32 v1, 0xda24260, v2
	v_cvt_f32_u32_e32 v2, s40
	s_sub_i32 s12, 32, s12
	v_mul_f32_e32 v1, 0x3c010204, v1
	s_lshl_b32 s69, s10, 6
	v_ldexp_f32 v2, v2, s12
	v_mul_f32_e32 v2, 0x2f800000, v2
	s_mov_b32 s12, 0x4ae00000
	v_div_scale_f32 v3, s[40:41], s12, s12, v2
	v_rcp_f32_e32 v4, v3
	s_lshl_b32 s10, s10, 13
	s_waitcnt vmcnt(2)
	s_barrier
	v_fma_f32 v5, -v3, v4, 1.0
	v_fmac_f32_e32 v4, v5, v4
	v_div_scale_f32 v5, vcc, v2, s12, v2
	v_mul_f32_e32 v6, v5, v4
	v_fma_f32 v7, -v3, v6, v5
	v_fmac_f32_e32 v6, v7, v4
	v_fma_f32 v3, -v3, v6, v5
	v_div_fmas_f32 v3, v3, v4, v6
	v_div_fixup_f32 v2, v3, s12, v2
	s_mov_b32 s12, 0xf800000
	v_cmp_gt_f32_e32 vcc, s12, v2
	v_mul_f32_e32 v3, 0x4f800000, v2
	s_movk_i32 s12, 0x3c0
	v_cndmask_b32_e32 v2, v2, v3, vcc
	v_sqrt_f32_e32 v3, v2
	s_mov_b32 s83, 0
	v_add_u32_e32 v4, -1, v3
	v_fma_f32 v5, -v4, v3, v2
	v_cmp_ge_f32_e64 s[40:41], 0, v5
	v_add_u32_e32 v5, 1, v3
	s_nop 0
	v_cndmask_b32_e64 v4, v3, v4, s[40:41]
	v_fma_f32 v3, -v5, v3, v2
	v_cmp_lt_f32_e64 s[40:41], 0, v3
	s_nop 1
	v_cndmask_b32_e64 v3, v4, v5, s[40:41]
	v_mul_f32_e32 v4, 0x37800000, v3
	v_cndmask_b32_e32 v3, v3, v4, vcc
	v_cmp_class_f32_e32 vcc, v2, v250
	s_nop 1
	v_cndmask_b32_e32 v2, v3, v2, vcc
	v_mul_f32_e32 v2, 0x40880000, v2
	v_max_f32_e32 v2, 0xda24260, v2
	v_mul_f32_e32 v2, 0x3c010204, v2
	v_mul_f32_e32 v1, v1, v2
	v_and_b32_e32 v2, 48, v0
	v_lshlrev_b32_e32 v3, 6, v0
	v_lshlrev_b32_e32 v0, 2, v0
	v_and_or_b32 v2, v3, s12, v2
	v_and_b32_e32 v0, 32, v0
	v_bitop3_b32 v3, v2, s10, v0 bitop3:0xde
	s_lshl_b32 s10, s11, 5
	s_and_b32 s70, s10, 0x60
	s_lshl_b32 s10, s70, 7
	v_bitop3_b32 v0, s10, v2, v0 bitop3:0xf6
	s_add_u32 s10, s54, 0x80
	s_addc_u32 s11, s55, 0
	s_add_i32 s71, s34, 0x18000
	s_mov_b32 m0, s71
	s_nop 0
	global_load_lds_dwordx4 v133, s[10:11]
	s_add_i32 s72, s34, 0x1a000
	s_mov_b32 m0, s72
	s_nop 0
	global_load_lds_dwordx4 v135, s[10:11]
	s_add_u32 s10, s56, 0x80
	s_addc_u32 s11, s57, 0
	s_add_i32 s78, s34, 0x8000
	s_mov_b32 m0, s78
	s_nop 0
	global_load_lds_dwordx4 v220, s[10:11]
	s_add_i32 s79, s34, 0xa000
	s_mov_b32 m0, s79
	s_nop 0
	global_load_lds_dwordx4 v221, s[10:11]
	s_add_u32 s10, s54, 0x40080
	s_addc_u32 s11, s55, 0
	s_add_i32 s80, s34, 0x1c000
	s_mov_b32 m0, s80
	s_nop 0
	global_load_lds_dwordx4 v133, s[10:11]
	s_add_i32 s81, s34, 0x1e000
	s_mov_b32 m0, s81
	s_nop 0
	global_load_lds_dwordx4 v135, s[10:11]
	s_waitcnt vmcnt(6)
	s_add_i32 s82, s34, 0xc000
	s_cmpk_lt_u32 s9, 0x100
	v_mul_f32_e32 v128, 0xbfb8aa3b, v1
	v_mul_f32_e32 v130, v1, v1
	s_cselect_b64 s[40:41], -1, 0
	v_mov_b32_e32 v129, v128
	v_mov_b32_e32 v131, v130
	v_add_u32_e32 v136, 0, v0
	v_add_u32_e32 v137, 0, v3
	s_barrier
	s_branch .LBB0_1304

.LBB0_1303:
	s_andn2_b64 vcc, exec, s[52:53]
	s_mov_b32 s85, s84
	s_mov_b32 s52, s42
	s_mov_b64 s[54:55], s[50:51]
	s_mov_b64 s[56:57], s[48:49]
	v_mov_b32_e32 v220, v224
	v_mov_b32_e32 v221, v225
	v_mov_b32_e32 v222, v226
	v_mov_b32_e32 v223, v227
	s_cbranch_vccz .LBB0_1315

.LBB0_1306:
	s_andn2_b64 vcc, exec, s[48:49]
	s_cbranch_vccnz .LBB0_1308
	s_ashr_i32 s10, s9, 31
	s_lshr_b32 s10, s10, 29
	s_add_i32 s10, s9, s10
	s_ashr_i32 s11, s10, 3
	s_and_b32 s10, s10, -8
	s_sub_i32 s9, s9, s10
	s_cmp_lt_i32 s9, 0
	s_cselect_b32 s10, s31, s30
	s_mul_i32 s9, s9, s10
	s_add_i32 s9, s9, s11
	s_mul_hi_i32 s10, s9, 0x92492493
	s_add_i32 s10, s10, s9
	s_lshr_b32 s11, s10, 31
	s_ashr_i32 s10, s10, 8
	s_add_i32 s10, s10, s11
	s_lshl_b32 s11, s10, 3
	s_sub_i32 s12, s27, s11
	s_min_i32 s12, s12, 8
	s_abs_i32 s42, s12
	v_cvt_f32_u32_e32 v0, s42
	s_sub_i32 s46, 0, s42
	s_mulk_i32 s10, 0x1c0
	s_sub_i32 s9, s9, s10
	v_rcp_iflag_f32_e32 v0, v0
	s_abs_i32 s10, s9
	s_xor_b32 s43, s9, s12
	s_ashr_i32 s43, s43, 31
	v_mul_f32_e32 v0, 0x4f7ffffe, v0
	v_cvt_u32_f32_e32 v0, v0
	s_nop 0
	v_readfirstlane_b32 s47, v0
	s_mul_i32 s46, s46, s47
	s_mul_hi_u32 s46, s47, s46
	s_add_i32 s47, s47, s46
	s_mul_hi_u32 s46, s10, s47
	s_mul_i32 s47, s46, s42
	s_sub_i32 s10, s10, s47
	s_add_i32 s48, s46, 1
	s_sub_i32 s47, s10, s42
	s_cmp_ge_u32 s10, s42
	s_cselect_b32 s46, s48, s46
	s_cselect_b32 s10, s47, s10
	s_add_i32 s47, s46, 1
	s_cmp_ge_u32 s10, s42
	s_cselect_b32 s10, s47, s46
	s_xor_b32 s10, s10, s43
	s_sub_i32 s84, s10, s43
	s_mul_i32 s10, s84, s12
	s_sub_i32 s9, s9, s10
	s_add_i32 s42, s11, s9
	s_ashr_i32 s43, s42, 31
	s_lshl_b64 s[10:11], s[42:43], 2
	s_add_u32 s10, s16, s10
	s_addc_u32 s11, s17, s11
	global_load_dword v0, v189, s[10:11] offset:768
	s_cmp_eq_u32 s42, s52
	s_cbranch_scc1 .Lgsk_a
	s_lshl_b32 s92, s42, 10
	s_add_u32 s10, s18, s92
	s_addc_u32 s11, s19, 0
	global_load_dword v224, v232, s[10:11]
	global_load_dword v225, v233, s[10:11]
	global_load_dword v226, v232, s[10:11] offset:512
	global_load_dword v227, v233, s[10:11] offset:512
.Lgsk_a:
	s_waitcnt vmcnt(0)
	s_cmp_eq_u32 s42, s52
	s_cbranch_scc1 .Lgsk_b
	s_lshl_b32 s92, s42, 19
	v_lshl_add_u32 v224, v224, 11, v234
	v_lshl_add_u32 v225, v225, 11, v235
	v_lshl_add_u32 v226, v226, 11, v234
	v_lshl_add_u32 v227, v227, 11, v235
	v_subrev_u32_e32 v224, s92, v224
	v_subrev_u32_e32 v225, s92, v225
	s_add_i32 s92, s92, 0x40000
	v_subrev_u32_e32 v226, s92, v226
	v_subrev_u32_e32 v227, s92, v227
	s_branch .Lgsk_c
.Lgsk_b:
	v_mov_b32_e32 v224, v220
	v_mov_b32_e32 v225, v221
	v_mov_b32_e32 v226, v222
	v_mov_b32_e32 v227, v223
.Lgsk_c:
	v_readfirstlane_b32 s9, v0
	s_mul_i32 s9, s9, 56
	s_add_i32 s46, s9, s84
.LBB0_1308:
	s_lshl_b64 s[10:11], s[42:43], 19
	s_add_u32 s48, s16, s10
	s_addc_u32 s49, s17, s11
	s_and_b64 s[10:11], exec, s[44:45]
	s_cselect_b32 s43, s49, s57
	s_cselect_b32 s53, s48, s56
	s_ashr_i32 s47, s46, 31
	s_lshl_b64 s[10:11], s[46:47], 19
	s_add_u32 s50, s28, s10
	s_addc_u32 s51, s29, s11
	s_and_b64 s[10:11], exec, s[44:45]
	s_cselect_b32 s47, s51, s55
	s_cselect_b32 s9, s50, s54
	s_add_u32 s10, s53, 0x80
	s_addc_u32 s11, s43, 0
	s_add_u32 s12, s9, 0x80
	s_addc_u32 s86, s47, 0
	s_mov_b32 s87, 0
	v_mov_b32_e32 v0, 0
	v_mov_b32_e32 v1, 0
	v_mov_b32_e32 v2, 0
	v_mov_b32_e32 v3, 0
	v_mov_b32_e32 v4, 0
	v_mov_b32_e32 v5, 0
	v_mov_b32_e32 v6, 0
	v_mov_b32_e32 v7, 0
	v_mov_b32_e32 v8, 0
	v_mov_b32_e32 v9, 0
	v_mov_b32_e32 v10, 0
	v_mov_b32_e32 v11, 0
	v_mov_b32_e32 v12, 0
	v_mov_b32_e32 v13, 0
	v_mov_b32_e32 v14, 0
	v_mov_b32_e32 v15, 0
	v_mov_b32_e32 v16, 0
	v_mov_b32_e32 v17, 0
	v_mov_b32_e32 v18, 0
	v_mov_b32_e32 v19, 0
	v_mov_b32_e32 v20, 0
	v_mov_b32_e32 v21, 0
	v_mov_b32_e32 v22, 0
	v_mov_b32_e32 v23, 0
	v_mov_b32_e32 v24, 0
	v_mov_b32_e32 v25, 0
	v_mov_b32_e32 v26, 0
	v_mov_b32_e32 v27, 0
	v_mov_b32_e32 v28, 0
	v_mov_b32_e32 v29, 0
	v_mov_b32_e32 v30, 0
	v_mov_b32_e32 v31, 0
	v_mov_b32_e32 v32, 0
	v_mov_b32_e32 v33, 0
	v_mov_b32_e32 v34, 0
	v_mov_b32_e32 v35, 0
	v_mov_b32_e32 v36, 0
	v_mov_b32_e32 v37, 0
	v_mov_b32_e32 v38, 0
	v_mov_b32_e32 v39, 0
	v_mov_b32_e32 v40, 0
	v_mov_b32_e32 v41, 0
	v_mov_b32_e32 v42, 0
	v_mov_b32_e32 v43, 0
	v_mov_b32_e32 v44, 0
	v_mov_b32_e32 v45, 0
	v_mov_b32_e32 v46, 0
	v_mov_b32_e32 v47, 0
	v_mov_b32_e32 v48, 0
	v_mov_b32_e32 v49, 0
	v_mov_b32_e32 v50, 0
	v_mov_b32_e32 v51, 0
	v_mov_b32_e32 v52, 0
	v_mov_b32_e32 v53, 0
	v_mov_b32_e32 v54, 0
	v_mov_b32_e32 v55, 0
	v_mov_b32_e32 v56, 0
	v_mov_b32_e32 v57, 0
	v_mov_b32_e32 v58, 0
	v_mov_b32_e32 v59, 0
	v_mov_b32_e32 v60, 0
	v_mov_b32_e32 v61, 0
	v_mov_b32_e32 v62, 0
	v_mov_b32_e32 v63, 0
	v_mov_b32_e32 v64, 0
	v_mov_b32_e32 v65, 0
	v_mov_b32_e32 v66, 0
	v_mov_b32_e32 v67, 0
	v_mov_b32_e32 v68, 0
	v_mov_b32_e32 v69, 0
	v_mov_b32_e32 v70, 0
	v_mov_b32_e32 v71, 0
	v_mov_b32_e32 v72, 0
	v_mov_b32_e32 v73, 0
	v_mov_b32_e32 v74, 0
	v_mov_b32_e32 v75, 0
	v_mov_b32_e32 v76, 0
	v_mov_b32_e32 v77, 0
	v_mov_b32_e32 v78, 0
	v_mov_b32_e32 v79, 0
	v_mov_b32_e32 v80, 0
	v_mov_b32_e32 v81, 0
	v_mov_b32_e32 v82, 0
	v_mov_b32_e32 v83, 0
	v_mov_b32_e32 v84, 0
	v_mov_b32_e32 v85, 0
	v_mov_b32_e32 v86, 0
	v_mov_b32_e32 v87, 0
	v_mov_b32_e32 v88, 0
	v_mov_b32_e32 v89, 0
	v_mov_b32_e32 v90, 0
	v_mov_b32_e32 v91, 0
	v_mov_b32_e32 v92, 0
	v_mov_b32_e32 v93, 0
	v_mov_b32_e32 v94, 0
	v_mov_b32_e32 v95, 0
	v_mov_b32_e32 v96, 0
	v_mov_b32_e32 v97, 0
	v_mov_b32_e32 v98, 0
	v_mov_b32_e32 v99, 0
	v_mov_b32_e32 v100, 0
	v_mov_b32_e32 v101, 0
	v_mov_b32_e32 v102, 0
	v_mov_b32_e32 v103, 0
	v_mov_b32_e32 v104, 0
	v_mov_b32_e32 v105, 0
	v_mov_b32_e32 v106, 0
	v_mov_b32_e32 v107, 0
	v_mov_b32_e32 v108, 0
	v_mov_b32_e32 v109, 0
	v_mov_b32_e32 v110, 0
	v_mov_b32_e32 v111, 0
	v_mov_b32_e32 v112, 0
	v_mov_b32_e32 v113, 0
	v_mov_b32_e32 v114, 0
	v_mov_b32_e32 v115, 0
	v_mov_b32_e32 v116, 0
	v_mov_b32_e32 v117, 0
	v_mov_b32_e32 v118, 0
	v_mov_b32_e32 v119, 0
	v_mov_b32_e32 v120, 0
	v_mov_b32_e32 v121, 0
	v_mov_b32_e32 v122, 0
	v_mov_b32_e32 v123, 0
	v_mov_b32_e32 v124, 0
	v_mov_b32_e32 v125, 0
	v_mov_b32_e32 v126, 0
	v_mov_b32_e32 v127, 0
	s_mov_b64 s[58:59], s[56:57]
.LBB0_1309:
	s_cmp_gt_u32 s87, 13
	s_cselect_b64 s[60:61], -1, 0
	s_and_b64 vcc, s[60:61], exec
	s_cselect_b32 s60, -14, 2
	s_add_i32 s60, s60, s87
	s_ashr_i32 s61, s60, 31
	s_lshl_b64 s[60:61], s[60:61], 7
	s_add_u32 s62, s56, s60
	s_addc_u32 s63, s57, s61
	s_add_u32 s76, s54, s60
	s_addc_u32 s77, s55, s61
	s_cmp_gt_u32 s87, 12
	s_cselect_b32 s60, -13, 3
	s_add_i32 s60, s60, s87
	s_ashr_i32 s61, s60, 31
	s_lshl_b64 s[60:61], s[60:61], 7
	s_add_u32 s88, s56, s60
	s_addc_u32 s89, s57, s61
	s_add_u32 s90, s54, s60
	s_mov_b32 s60, s87
	v_add_u32_e32 v150, 0x10000, v136
	v_add_u32_e32 v166, 0x14000, v136
	ds_read_b128 v[138:141], v150
	ds_read_b128 v[142:145], v150 offset:1024
	ds_read_b128 v[146:149], v150 offset:2048
	ds_read_b128 v[150:153], v150 offset:3072
	ds_read_b128 v[154:157], v166
	ds_read_b128 v[158:161], v166 offset:1024
	ds_read_b128 v[162:165], v166 offset:2048
	ds_read_b128 v[166:169], v166 offset:3072
	s_addc_u32 s91, s55, s61
	s_cmp_eq_u32 s87, 14
	s_cselect_b64 s[98:99], -1, 0
	s_cselect_b32 s75, s43, s63
	s_cselect_b32 s74, s53, s62
	s_cselect_b32 s77, s47, s77
	s_cselect_b32 s76, s9, s76
	s_cselect_b32 s61, s11, s89
	s_cselect_b32 s60, s10, s88
	s_cselect_b32 s63, s86, s91
	s_cselect_b32 s62, s12, s90
	ds_read_b128 v[170:173], v137
	ds_read_b128 v[174:177], v137 offset:1024
	ds_read_b128 v[178:181], v137 offset:2048
	ds_read_b128 v[182:185], v137 offset:3072
	ds_read_b128 v[190:193], v137 offset:4096
	ds_read_b128 v[194:197], v137 offset:5120
	ds_read_b128 v[198:201], v137 offset:6144
	ds_read_b128 v[202:205], v137 offset:7168
	v_cndmask_b32_e64 v228, v220, v224, s[98:99]
	v_cndmask_b32_e64 v229, v221, v225, s[98:99]
	v_cndmask_b32_e64 v230, v222, v226, s[98:99]
	v_cndmask_b32_e64 v231, v223, v227, s[98:99]
	s_add_u32 s88, s58, 0x40080
	s_addc_u32 s89, s59, 0
	s_mov_b32 m0, s82
	s_nop 0
	global_load_lds_dwordx4 v222, s[88:89]
	s_add_i32 s90, s34, 0xe000
	s_mov_b32 m0, s90
	s_nop 0
	global_load_lds_dwordx4 v223, s[88:89]
	s_setprio 1
	s_waitcnt vmcnt(8)
	s_waitcnt lgkmcnt(0)
	s_barrier
	v_mfma_i32_16x16x64_i8 v[124:127], v[138:141], v[170:173], v[124:127]
	v_mfma_i32_16x16x64_i8 v[120:123], v[146:149], v[170:173], v[120:123]
	v_mfma_i32_16x16x64_i8 v[116:119], v[138:141], v[178:181], v[116:119]
	v_mfma_i32_16x16x64_i8 v[112:115], v[146:149], v[178:181], v[112:115]
	v_mfma_i32_16x16x64_i8 v[108:111], v[138:141], v[190:193], v[108:111]
	v_mfma_i32_16x16x64_i8 v[104:107], v[146:149], v[190:193], v[104:107]
	v_mfma_i32_16x16x64_i8 v[100:103], v[138:141], v[198:201], v[100:103]
	v_mfma_i32_16x16x64_i8 v[96:99], v[146:149], v[198:201], v[96:99]
	v_mfma_i32_16x16x64_i8 v[124:127], v[142:145], v[174:177], v[124:127]
	v_mfma_i32_16x16x64_i8 v[120:123], v[150:153], v[174:177], v[120:123]
	v_mfma_i32_16x16x64_i8 v[116:119], v[142:145], v[182:185], v[116:119]
	v_mfma_i32_16x16x64_i8 v[112:115], v[150:153], v[182:185], v[112:115]
	v_mfma_i32_16x16x64_i8 v[108:111], v[142:145], v[194:197], v[108:111]
	v_mfma_i32_16x16x64_i8 v[104:107], v[150:153], v[194:197], v[104:107]
	v_mfma_i32_16x16x64_i8 v[100:103], v[142:145], v[202:205], v[100:103]
	v_mfma_i32_16x16x64_i8 v[96:99], v[150:153], v[202:205], v[96:99]
	v_mfma_i32_16x16x64_i8 v[92:95], v[154:157], v[170:173], v[92:95]
	v_mfma_i32_16x16x64_i8 v[88:91], v[162:165], v[170:173], v[88:91]
	v_mfma_i32_16x16x64_i8 v[84:87], v[154:157], v[178:181], v[84:87]
	v_mfma_i32_16x16x64_i8 v[80:83], v[162:165], v[178:181], v[80:83]
	v_mfma_i32_16x16x64_i8 v[76:79], v[154:157], v[190:193], v[76:79]
	v_mfma_i32_16x16x64_i8 v[72:75], v[162:165], v[190:193], v[72:75]
	v_mfma_i32_16x16x64_i8 v[68:71], v[154:157], v[198:201], v[68:71]
	v_mfma_i32_16x16x64_i8 v[64:67], v[162:165], v[198:201], v[64:67]
	v_mfma_i32_16x16x64_i8 v[92:95], v[158:161], v[174:177], v[92:95]
	v_mfma_i32_16x16x64_i8 v[88:91], v[166:169], v[174:177], v[88:91]
	v_mfma_i32_16x16x64_i8 v[84:87], v[158:161], v[182:185], v[84:87]
	v_mfma_i32_16x16x64_i8 v[80:83], v[166:169], v[182:185], v[80:83]
	v_mfma_i32_16x16x64_i8 v[76:79], v[158:161], v[194:197], v[76:79]
	v_mfma_i32_16x16x64_i8 v[72:75], v[166:169], v[194:197], v[72:75]
	v_mfma_i32_16x16x64_i8 v[68:71], v[158:161], v[202:205], v[68:71]
	v_mfma_i32_16x16x64_i8 v[64:67], v[166:169], v[202:205], v[64:67]
	s_barrier
	s_setprio 0
	ds_read_b128 v[170:173], v137 offset:16384
	ds_read_b128 v[174:177], v137 offset:17408
	ds_read_b128 v[178:181], v137 offset:18432
	ds_read_b128 v[182:185], v137 offset:19456
	ds_read_b128 v[190:193], v137 offset:20480
	ds_read_b128 v[194:197], v137 offset:21504
	ds_read_b128 v[198:201], v137 offset:22528
	ds_read_b128 v[202:205], v137 offset:23552
	s_mov_b32 m0, s35
	s_nop 0
	global_load_lds_dwordx4 v133, s[76:77]
	s_nop 0
	s_mov_b32 m0, s36
	s_nop 0
	global_load_lds_dwordx4 v135, s[76:77]
	s_add_u32 s76, s76, 0x40000
	s_addc_u32 s77, s77, 0
	s_mov_b32 m0, s37
	s_nop 0
	global_load_lds_dwordx4 v133, s[76:77]
	s_nop 0
	s_mov_b32 m0, s65
	s_nop 0
	global_load_lds_dwordx4 v135, s[76:77]
	s_mov_b32 m0, s34
	s_nop 0
	global_load_lds_dwordx4 v228, s[74:75]
	s_nop 0
	s_mov_b32 m0, s66
	s_nop 0
	global_load_lds_dwordx4 v229, s[74:75]
	s_setprio 1
	s_waitcnt vmcnt(8)
	s_waitcnt lgkmcnt(0)
	s_barrier
	v_mfma_i32_16x16x64_i8 v[60:63], v[138:141], v[170:173], v[60:63]
	v_mfma_i32_16x16x64_i8 v[56:59], v[146:149], v[170:173], v[56:59]
	v_mfma_i32_16x16x64_i8 v[52:55], v[138:141], v[178:181], v[52:55]
	v_mfma_i32_16x16x64_i8 v[48:51], v[146:149], v[178:181], v[48:51]
	v_mfma_i32_16x16x64_i8 v[44:47], v[138:141], v[190:193], v[44:47]
	v_mfma_i32_16x16x64_i8 v[40:43], v[146:149], v[190:193], v[40:43]
	v_mfma_i32_16x16x64_i8 v[36:39], v[138:141], v[198:201], v[36:39]
	v_mfma_i32_16x16x64_i8 v[32:35], v[146:149], v[198:201], v[32:35]
	v_mfma_i32_16x16x64_i8 v[60:63], v[142:145], v[174:177], v[60:63]
	v_mfma_i32_16x16x64_i8 v[56:59], v[150:153], v[174:177], v[56:59]
	v_mfma_i32_16x16x64_i8 v[52:55], v[142:145], v[182:185], v[52:55]
	v_mfma_i32_16x16x64_i8 v[48:51], v[150:153], v[182:185], v[48:51]
	v_mfma_i32_16x16x64_i8 v[44:47], v[142:145], v[194:197], v[44:47]
	v_mfma_i32_16x16x64_i8 v[40:43], v[150:153], v[194:197], v[40:43]
	v_mfma_i32_16x16x64_i8 v[36:39], v[142:145], v[202:205], v[36:39]
	v_mfma_i32_16x16x64_i8 v[32:35], v[150:153], v[202:205], v[32:35]
	v_mfma_i32_16x16x64_i8 v[28:31], v[154:157], v[170:173], v[28:31]
	v_mfma_i32_16x16x64_i8 v[24:27], v[162:165], v[170:173], v[24:27]
	v_mfma_i32_16x16x64_i8 v[20:23], v[154:157], v[178:181], v[20:23]
	v_mfma_i32_16x16x64_i8 v[16:19], v[162:165], v[178:181], v[16:19]
	v_mfma_i32_16x16x64_i8 v[12:15], v[154:157], v[190:193], v[12:15]
	v_mfma_i32_16x16x64_i8 v[8:11], v[162:165], v[190:193], v[8:11]
	v_mfma_i32_16x16x64_i8 v[4:7], v[154:157], v[198:201], v[4:7]
	v_mfma_i32_16x16x64_i8 v[0:3], v[162:165], v[198:201], v[0:3]
	v_mfma_i32_16x16x64_i8 v[28:31], v[158:161], v[174:177], v[28:31]
	v_mfma_i32_16x16x64_i8 v[24:27], v[166:169], v[174:177], v[24:27]
	v_mfma_i32_16x16x64_i8 v[20:23], v[158:161], v[182:185], v[20:23]
	v_mfma_i32_16x16x64_i8 v[16:19], v[166:169], v[182:185], v[16:19]
	v_mfma_i32_16x16x64_i8 v[12:15], v[158:161], v[194:197], v[12:15]
	v_mfma_i32_16x16x64_i8 v[8:11], v[166:169], v[194:197], v[8:11]
	v_mfma_i32_16x16x64_i8 v[4:7], v[158:161], v[202:205], v[4:7]
	v_mfma_i32_16x16x64_i8 v[0:3], v[166:169], v[202:205], v[0:3]
	s_barrier
	s_setprio 0
	v_add_u32_e32 v150, 0x18000, v136
	v_add_u32_e32 v166, 0x1c000, v136
	ds_read_b128 v[138:141], v150
	ds_read_b128 v[142:145], v150 offset:1024
	ds_read_b128 v[146:149], v150 offset:2048
	ds_read_b128 v[150:153], v150 offset:3072
	ds_read_b128 v[154:157], v166
	ds_read_b128 v[158:161], v166 offset:1024
	ds_read_b128 v[162:165], v166 offset:2048
	ds_read_b128 v[166:169], v166 offset:3072
	ds_read_b128 v[170:173], v137 offset:32768
	ds_read_b128 v[174:177], v137 offset:33792
	ds_read_b128 v[178:181], v137 offset:34816
	ds_read_b128 v[182:185], v137 offset:35840
	ds_read_b128 v[190:193], v137 offset:36864
	ds_read_b128 v[194:197], v137 offset:37888
	ds_read_b128 v[198:201], v137 offset:38912
	ds_read_b128 v[202:205], v137 offset:39936
	s_add_u32 s74, s74, 0x40000
	s_addc_u32 s75, s75, 0
	s_mov_b32 m0, s67
	s_nop 0
	global_load_lds_dwordx4 v230, s[74:75]
	s_nop 0
	s_mov_b32 m0, s68
	s_nop 0
	global_load_lds_dwordx4 v231, s[74:75]
	s_setprio 1
	s_waitcnt vmcnt(8)
	s_waitcnt lgkmcnt(0)
	s_barrier
	v_mfma_i32_16x16x64_i8 v[124:127], v[138:141], v[170:173], v[124:127]
	v_mfma_i32_16x16x64_i8 v[120:123], v[146:149], v[170:173], v[120:123]
	v_mfma_i32_16x16x64_i8 v[116:119], v[138:141], v[178:181], v[116:119]
	v_mfma_i32_16x16x64_i8 v[112:115], v[146:149], v[178:181], v[112:115]
	v_mfma_i32_16x16x64_i8 v[108:111], v[138:141], v[190:193], v[108:111]
	v_mfma_i32_16x16x64_i8 v[104:107], v[146:149], v[190:193], v[104:107]
	v_mfma_i32_16x16x64_i8 v[100:103], v[138:141], v[198:201], v[100:103]
	v_mfma_i32_16x16x64_i8 v[96:99], v[146:149], v[198:201], v[96:99]
	v_mfma_i32_16x16x64_i8 v[124:127], v[142:145], v[174:177], v[124:127]
	v_mfma_i32_16x16x64_i8 v[120:123], v[150:153], v[174:177], v[120:123]
	v_mfma_i32_16x16x64_i8 v[116:119], v[142:145], v[182:185], v[116:119]
	v_mfma_i32_16x16x64_i8 v[112:115], v[150:153], v[182:185], v[112:115]
	v_mfma_i32_16x16x64_i8 v[108:111], v[142:145], v[194:197], v[108:111]
	v_mfma_i32_16x16x64_i8 v[104:107], v[150:153], v[194:197], v[104:107]
	v_mfma_i32_16x16x64_i8 v[100:103], v[142:145], v[202:205], v[100:103]
	v_mfma_i32_16x16x64_i8 v[96:99], v[150:153], v[202:205], v[96:99]
	v_mfma_i32_16x16x64_i8 v[92:95], v[154:157], v[170:173], v[92:95]
	v_mfma_i32_16x16x64_i8 v[88:91], v[162:165], v[170:173], v[88:91]
	v_mfma_i32_16x16x64_i8 v[84:87], v[154:157], v[178:181], v[84:87]
	v_mfma_i32_16x16x64_i8 v[80:83], v[162:165], v[178:181], v[80:83]
	v_mfma_i32_16x16x64_i8 v[76:79], v[154:157], v[190:193], v[76:79]
	v_mfma_i32_16x16x64_i8 v[72:75], v[162:165], v[190:193], v[72:75]
	v_mfma_i32_16x16x64_i8 v[68:71], v[154:157], v[198:201], v[68:71]
	v_mfma_i32_16x16x64_i8 v[64:67], v[162:165], v[198:201], v[64:67]
	v_mfma_i32_16x16x64_i8 v[92:95], v[158:161], v[174:177], v[92:95]
	v_mfma_i32_16x16x64_i8 v[88:91], v[166:169], v[174:177], v[88:91]
	v_mfma_i32_16x16x64_i8 v[84:87], v[158:161], v[182:185], v[84:87]
	v_mfma_i32_16x16x64_i8 v[80:83], v[166:169], v[182:185], v[80:83]
	v_mfma_i32_16x16x64_i8 v[76:79], v[158:161], v[194:197], v[76:79]
	v_mfma_i32_16x16x64_i8 v[72:75], v[166:169], v[194:197], v[72:75]
	v_mfma_i32_16x16x64_i8 v[68:71], v[158:161], v[202:205], v[68:71]
	v_mfma_i32_16x16x64_i8 v[64:67], v[166:169], v[202:205], v[64:67]
	s_barrier
	s_setprio 0
	ds_read_b128 v[170:173], v137 offset:49152
	ds_read_b128 v[174:177], v137 offset:50176
	ds_read_b128 v[178:181], v137 offset:51200
	ds_read_b128 v[182:185], v137 offset:52224
	ds_read_b128 v[190:193], v137 offset:53248
	ds_read_b128 v[194:197], v137 offset:54272
	ds_read_b128 v[198:201], v137 offset:55296
	ds_read_b128 v[202:205], v137 offset:56320
	s_mov_b32 m0, s71
	s_nop 0
	global_load_lds_dwordx4 v133, s[62:63]
	s_nop 0
	s_mov_b32 m0, s72
	s_nop 0
	global_load_lds_dwordx4 v135, s[62:63]
	s_add_u32 s62, s62, 0x40000
	s_addc_u32 s63, s63, 0
	s_mov_b32 m0, s80
	s_nop 0
	global_load_lds_dwordx4 v133, s[62:63]
	s_nop 0
	s_mov_b32 m0, s81
	s_nop 0
	global_load_lds_dwordx4 v135, s[62:63]
	s_mov_b32 m0, s78
	s_nop 0
	global_load_lds_dwordx4 v228, s[60:61]
	s_nop 0
	s_mov_b32 m0, s79
	s_nop 0
	global_load_lds_dwordx4 v229, s[60:61]
	s_setprio 1
	s_waitcnt vmcnt(8)
	s_waitcnt lgkmcnt(0)
	s_barrier
	v_mfma_i32_16x16x64_i8 v[60:63], v[138:141], v[170:173], v[60:63]
	v_mfma_i32_16x16x64_i8 v[56:59], v[146:149], v[170:173], v[56:59]
	v_mfma_i32_16x16x64_i8 v[52:55], v[138:141], v[178:181], v[52:55]
	v_mfma_i32_16x16x64_i8 v[48:51], v[146:149], v[178:181], v[48:51]
	v_mfma_i32_16x16x64_i8 v[44:47], v[138:141], v[190:193], v[44:47]
	v_mfma_i32_16x16x64_i8 v[40:43], v[146:149], v[190:193], v[40:43]
	v_mfma_i32_16x16x64_i8 v[36:39], v[138:141], v[198:201], v[36:39]
	v_mfma_i32_16x16x64_i8 v[32:35], v[146:149], v[198:201], v[32:35]
	v_mfma_i32_16x16x64_i8 v[60:63], v[142:145], v[174:177], v[60:63]
	v_mfma_i32_16x16x64_i8 v[56:59], v[150:153], v[174:177], v[56:59]
	v_mfma_i32_16x16x64_i8 v[52:55], v[142:145], v[182:185], v[52:55]
	v_mfma_i32_16x16x64_i8 v[48:51], v[150:153], v[182:185], v[48:51]
	v_mfma_i32_16x16x64_i8 v[44:47], v[142:145], v[194:197], v[44:47]
	v_mfma_i32_16x16x64_i8 v[40:43], v[150:153], v[194:197], v[40:43]
	v_mfma_i32_16x16x64_i8 v[36:39], v[142:145], v[202:205], v[36:39]
	v_mfma_i32_16x16x64_i8 v[32:35], v[150:153], v[202:205], v[32:35]
	v_mfma_i32_16x16x64_i8 v[28:31], v[154:157], v[170:173], v[28:31]
	v_mfma_i32_16x16x64_i8 v[24:27], v[162:165], v[170:173], v[24:27]
	v_mfma_i32_16x16x64_i8 v[20:23], v[154:157], v[178:181], v[20:23]
	v_mfma_i32_16x16x64_i8 v[16:19], v[162:165], v[178:181], v[16:19]
	v_mfma_i32_16x16x64_i8 v[12:15], v[154:157], v[190:193], v[12:15]
	v_mfma_i32_16x16x64_i8 v[8:11], v[162:165], v[190:193], v[8:11]
	v_mfma_i32_16x16x64_i8 v[4:7], v[154:157], v[198:201], v[4:7]
	v_mfma_i32_16x16x64_i8 v[0:3], v[162:165], v[198:201], v[0:3]
	v_mfma_i32_16x16x64_i8 v[28:31], v[158:161], v[174:177], v[28:31]
	v_mfma_i32_16x16x64_i8 v[24:27], v[166:169], v[174:177], v[24:27]
	v_mfma_i32_16x16x64_i8 v[20:23], v[158:161], v[182:185], v[20:23]
	v_mfma_i32_16x16x64_i8 v[16:19], v[166:169], v[182:185], v[16:19]
	v_mfma_i32_16x16x64_i8 v[12:15], v[158:161], v[194:197], v[12:15]
	v_mfma_i32_16x16x64_i8 v[8:11], v[166:169], v[194:197], v[8:11]
	v_mfma_i32_16x16x64_i8 v[4:7], v[158:161], v[202:205], v[4:7]
	v_mfma_i32_16x16x64_i8 v[0:3], v[166:169], v[202:205], v[0:3]
	s_barrier
	s_setprio 0
	s_add_i32 s87, s87, 2
	s_add_u32 s58, s58, 0x100
	s_addc_u32 s59, s59, 0
	s_cbranch_vccz .LBB0_1309
	s_and_b64 vcc, exec, s[40:41]
	s_cbranch_vccz .LBB0_1312
	s_barrier
